# karg100
# speedup vs baseline: 1.0020x; 1.0020x over previous
_Z11prep_kernelPKfS0_PKiS2_S0_S0_S0_S0_S0_S0_Pc:
	s_getpc_b64 s[36:37]
	s_add_u32 s36, s36, _Z11attn_kernelILi4EEvPKfS1_S1_S1_S1_S1_PKcPf@rel32@lo+4
	s_addc_u32 s37, s37, _Z11attn_kernelILi4EEvPKfS1_S1_S1_S1_S1_PKcPf@rel32@hi+12
	v_and_b32_e32 v192, 63, v0
	v_lshlrev_b32_e32 v192, 7, v192
	v_min_u32_e32 v192, 0x1180, v192
	global_load_dword v192, v192, s[36:37]
	s_lshr_b32 s4, s2, 2
	v_lshrrev_b32_e32 v2, 6, v0
	s_and_b32 s4, s4, 0x1ffffffe
	s_load_dwordx4 s[28:31], s[0:1], 0x40
	s_load_dwordx8 s[12:19], s[0:1], 0x0
	s_load_dwordx8 s[20:27], s[0:1], 0x20
	s_load_dwordx2 s[32:33], s[0:1], 0x50
	s_load_dword s40, s[0:1], 0x100
	v_and_b32_e32 v1, 15, v0
	s_and_b32 s3, s2, 7
	v_or_b32_e32 v2, s4, v2
	v_lshl_or_b32 v88, v2, 3, s3
	v_cmp_gt_u32_e64 s[10:11], 14, v1
	v_mul_lo_u32 v7, v88, 14
	v_and_b32_e32 v105, 63, v0
	v_cndmask_b32_e64 v6, 13, v1, s[10:11]
	v_add_u32_e32 v2, v7, v6
	v_mul_u32_u24_e32 v4, 12, v2
	v_lshlrev_b32_e32 v5, 2, v6
	v_cmp_gt_u32_e64 s[8:9], 48, v105
	v_cmp_gt_u32_e64 s[6:7], 14, v105
	v_lshlrev_b32_e32 v118, 1, v0
	v_lshrrev_b32_e32 v104, 4, v0
	v_cndmask_b32_e64 v8, 0, v105, s[8:9]
	v_cndmask_b32_e64 v9, 0, v105, s[6:7]
	v_mad_u32_u24 v8, v88, 48, v8
	v_add_lshl_u32 v9, v7, v9, 2
	v_lshlrev_b32_e32 v8, 2, v8
	s_lshl_b32 s2, s2, 3
	s_and_b32 s2, s2, 0x78
	v_and_b32_e32 v106, 30, v118
	v_or_b32_e32 v107, s2, v104
	v_cmp_gt_u32_e64 s[2:3], 23, v106
	v_or_b32_e32 v10, 1, v106
	v_cmp_gt_u32_e64 s[4:5], 23, v10
	v_lshlrev_b32_e32 v11, 7, v106
	v_lshlrev_b32_e32 v10, 7, v10
	v_cndmask_b32_e64 v11, 0, v11, s[2:3]
	v_cndmask_b32_e64 v10, 0, v10, s[4:5]
	v_or_b32_e32 v11, v11, v107
	v_or_b32_e32 v10, v10, v107
	v_lshlrev_b32_e32 v11, 2, v11
	v_lshlrev_b32_e32 v10, 2, v10
	v_lshlrev_b32_e32 v12, 2, v107
	v_lshlrev_b32_e32 v119, 5, v0
	v_lshlrev_b32_e32 v13, 2, v0
	v_and_b32_e32 v109, 12, v13
	v_and_b32_e32 v91, 0xf80, v119
	v_lshl_or_b32 v91, v109, 2, v91
	v_or_b32_e32 v92, 0x1000, v91
	v_lshlrev_b32_e32 v90, 9, v2
	v_and_b32_e32 v16, 48, v0
	v_or_b32_e32 v90, v90, v16
	v_or_b32_e32 v112, 0x80, v0
	v_or_b32_e32 v111, 0x180, v0
	v_or_b32_e32 v108, 0x280, v0
	v_mov_b32_e32 v87, 0
	v_bfe_u32 v110, v0, 4, 2
	s_movk_i32 s34, 0x60
	v_lshrrev_b32_e32 v136, 1, v0
	v_lshrrev_b32_e32 v18, 3, v0
	v_and_b32_e32 v18, 4, v18
	v_and_b32_e32 v19, 24, v0
	v_and_b32_e32 v20, 2, v136
	v_or3_b32 v18, v18, v19, v20
	v_and_or_b32 v136, v136, s34, v18
	v_mul_u32_u24_e32 v18, 0x110, v109
	v_lshl_add_u32 v136, v136, 1, v18
	v_add_u32_e32 v137, 0x1100, v136
	v_add_u32_e32 v138, 0x2200, v136
	v_lshlrev_b32_e32 v18, 9, v88
	v_and_b32_e32 v19, 0x100, v119
	v_lshlrev_b32_e32 v20, 4, v0
	v_and_b32_e32 v20, 48, v20
	v_or3_b32 v139, v18, v19, v20
	v_and_b32_e32 v19, 8, v118
	v_and_b32_e32 v20, 64, v118
	v_or3_b32 v139, v139, v19, v20
	v_lshlrev_b32_e32 v19, 2, v110
	v_and_b32_e32 v20, 4, v19
	v_or_b32_e32 v139, v139, v20
	v_lshl_or_b32 v140, v1, 5, v18
	v_or_b32_e32 v140, v140, v19
	v_add_u32_e32 v140, 0x80000, v140
	v_lshl_or_b32 v141, v88, 4, v1
	v_lshlrev_b32_e32 v141, 3, v141
	v_add_u32_e32 v141, 0x140000, v141
	v_lshlrev_b32_e32 v20, 8, v88
	v_mul_u32_u24_e32 v21, 43, v105
	v_lshrrev_b32_e32 v21, 9, v21
	v_mul_u32_u24_e32 v21, 12, v21
	v_sub_u32_e32 v22, v105, v21
	v_and_b32_e32 v142, 3, v22
	v_lshrrev_b32_e32 v22, 2, v22
	v_mad_u32_u24 v142, v142, 3, v22
	v_add_u32_e32 v142, v142, v21
	v_lshl_add_u32 v142, v142, 2, v20
	v_add_u32_e32 v142, 0x164000, v142
	v_lshl_add_u32 v143, v105, 2, v20
	v_add_u32_e32 v143, 0x164000, v143
	v_lshlrev_b32_e32 v123, 6, v107
	v_lshl_add_u32 v123, v106, 1, v123
	v_add_u32_e32 v123, 0x160000, v123
	v_lshl_add_u32 v122, v1, 4, v20
	v_or_b32_e32 v122, v122, v19
	v_add_u32_e32 v122, 0x100000, v122
	s_waitcnt lgkmcnt(0)
	global_load_dwordx3 v[82:84], v4, s[12:13]
	global_load_dword v85, v5, s[26:27]
	global_load_dword v114, v8, s[18:19]
	global_load_dword v115, v9, s[16:17]
	global_load_dword v116, v11, s[28:29]
	global_load_dword v113, v10, s[28:29]
	global_load_dword v117, v12, s[30:31]
	global_load_dwordx4 v[66:69], v91, s[20:21]
	global_load_dwordx4 v[70:73], v91, s[20:21] offset:64
	global_load_dwordx4 v[74:77], v92, s[20:21]
	global_load_dwordx4 v[78:81], v92, s[20:21] offset:64
	global_load_dwordx4 v[58:61], v91, s[22:23]
	global_load_dwordx4 v[62:65], v91, s[22:23] offset:64
	global_load_dwordx4 v[50:53], v92, s[22:23]
	global_load_dwordx4 v[54:57], v92, s[22:23] offset:64
	global_load_dwordx4 v[42:45], v91, s[24:25]
	global_load_dwordx4 v[46:49], v91, s[24:25] offset:64
	global_load_dwordx4 v[34:37], v92, s[24:25]
	global_load_dwordx4 v[38:41], v92, s[24:25] offset:64
	global_load_dwordx4 v[26:29], v90, s[14:15] nt
	global_load_dwordx4 v[30:33], v90, s[14:15] offset:64 nt
	global_load_dwordx4 v[18:21], v90, s[14:15] offset:128 nt
	global_load_dwordx4 v[22:25], v90, s[14:15] offset:192 nt
	global_load_dwordx4 v[10:13], v90, s[14:15] offset:256 nt
	global_load_dwordx4 v[14:17], v90, s[14:15] offset:320 nt
	global_load_dwordx4 v[2:5], v90, s[14:15] offset:384 nt
	global_load_dwordx4 v[6:9], v90, s[14:15] offset:448 nt
	s_waitcnt vmcnt(26)
	v_mov_b32_e32 v90, v83
	v_mov_b32_e32 v91, v84
	v_lshlrev_b32_e32 v86, 2, v110
	s_waitcnt vmcnt(25)
	v_mul_f32_e32 v84, 0x3fb8aa3b, v85
	s_mov_b32 s14, 0x41700000
	v_exp_f32_e32 v84, v84
	v_cndmask_b32_e64 v94, 0, 1.0, s[10:11]
	v_add_f32_e32 v84, 1.0, v84
	v_cmp_lt_f32_e32 vcc, s14, v85
	v_log_f32_e32 v84, v84
	v_cmp_lt_u32_e64 s[12:13], 15, v105
	v_mul_f32_e32 v84, 0x3f317218, v84
	v_cndmask_b32_e32 v84, v84, v85, vcc
	v_mul_f32_e32 v84, 0xbe715bef, v84
	v_mul_f32_e32 v84, 0x3f3504f3, v84
	v_mul_f32_e32 v84, 0x41800000, v84
	v_cndmask_b32_e64 v99, 0, v84, s[10:11]
	v_mul_f32_e32 v101, -2.0, v99
	v_mul_f32_e32 v100, v82, v82
	v_cmp_gt_u32_e32 vcc, 16, v105
	v_fmac_f32_e32 v100, v90, v90
	v_cmp_eq_u32_e64 s[12:13], 0, v110
	v_fmac_f32_e32 v100, v91, v91
	v_cmp_eq_u32_e64 s[14:15], 1, v110
	v_mul_f32_e32 v83, v101, v82
	v_cmp_eq_u32_e64 s[16:17], 2, v110
	v_mul_f32_e32 v84, v101, v90
	v_mul_f32_e32 v85, v101, v91
	v_mul_f32_e32 v89, v99, v100
	v_mul_f32_e32 v92, v82, v94
	v_mul_f32_e32 v93, v90, v94
	v_mul_f32_e32 v95, v91, v94
	v_mul_f32_e32 v96, v100, v94
	v_cvt_pk_fp8_f32 v88, v83, v83
	v_cvt_pk_fp8_f32 v104, v84, v84
	v_cvt_f32_fp8_e32 v97, v88
	v_cvt_f32_fp8_e32 v98, v104
	v_sub_f32_e32 v97, v83, v97
	v_sub_f32_e32 v98, v84, v98
	v_cvt_pk_fp8_f32 v88, v85, v85
	v_cvt_pk_fp8_f32 v104, v99, v99
	v_cvt_f32_fp8_e32 v101, v88
	v_cvt_f32_fp8_e32 v102, v104
	v_sub_f32_e32 v101, v85, v101
	v_sub_f32_e32 v102, v99, v102
	v_cvt_pk_fp8_f32 v88, v89, v89
	v_cvt_pk_fp8_f32 v104, v92, v92
	v_cvt_f32_fp8_e32 v103, v88
	v_cvt_f32_fp8_e32 v120, v104
	v_sub_f32_e32 v103, v89, v103
	v_sub_f32_e32 v120, v92, v120
	v_cvt_pk_fp8_f32 v88, v93, v93
	v_cvt_pk_fp8_f32 v104, v95, v95
	v_cvt_f32_fp8_e32 v121, v88
	v_cvt_f32_fp8_e32 v86, v104
	v_sub_f32_e32 v121, v93, v121
	v_sub_f32_e32 v86, v95, v86
	v_cvt_pk_fp8_f32 v88, v96, v96
	s_nop 0
	v_cvt_f32_fp8_e32 v87, v88
	s_nop 0
	v_sub_f32_e32 v87, v96, v87
	v_cndmask_b32_e64 v124, v89, v85, s[16:17]
	v_cndmask_b32_e64 v124, v124, v98, s[14:15]
	v_cndmask_b32_e64 v124, v124, v83, s[12:13]
	v_cndmask_b32_e64 v125, v103, v99, s[16:17]
	v_cndmask_b32_e64 v125, v125, v84, s[14:15]
	v_cndmask_b32_e64 v125, v125, v97, s[12:13]
	v_cndmask_b32_e64 v126, 0, v102, s[16:17]
	v_cndmask_b32_e64 v126, v126, v85, s[14:15]
	v_cndmask_b32_e64 v126, v126, v83, s[12:13]
	v_cndmask_b32_e64 v127, 0, v99, s[16:17]
	v_cndmask_b32_e64 v127, v127, v101, s[14:15]
	v_cndmask_b32_e64 v127, v127, v84, s[12:13]
	v_cndmask_b32_e64 v128, v94, v86, s[16:17]
	v_cndmask_b32_e64 v128, v128, v93, s[14:15]
	v_cndmask_b32_e64 v128, v128, v92, s[12:13]
	v_cndmask_b32_e64 v129, v94, v96, s[16:17]
	v_cndmask_b32_e64 v129, v129, v121, s[14:15]
	v_cndmask_b32_e64 v129, v129, v92, s[12:13]
	v_cndmask_b32_e64 v130, 0, v96, s[16:17]
	v_cndmask_b32_e64 v130, v130, v95, s[14:15]
	v_cndmask_b32_e64 v130, v130, v120, s[12:13]
	v_cndmask_b32_e64 v131, 0, v87, s[16:17]
	v_cndmask_b32_e64 v131, v131, v95, s[14:15]
	v_cndmask_b32_e64 v131, v131, v93, s[12:13]
	v_cvt_pk_fp8_f32 v119, v124, v125
	v_cvt_pk_fp8_f32 v103, v128, v129
	v_cvt_pk_fp8_f32 v119, v126, v127 op_sel:[0,0,1]
	v_cvt_pk_fp8_f32 v103, v130, v131 op_sel:[0,0,1]
	s_nop 0
	global_store_dword v139, v119, s[32:33] offset:128
	global_store_dword v140, v103, s[32:33] offset:16
	s_and_saveexec_b64 s[0:1], vcc
	s_cbranch_execz .LBB0_14
	v_cvt_f16_f32_e32 v83, v82
	v_cvt_pk_f16_f32 v90, v90, v91
	s_nop 0
	v_alignbit_b32 v91, 0, v90, 16
	v_pack_b32_f16 v90, v83, v90
	global_store_dwordx2 v141, v[90:91], s[32:33]
